# speedup vs baseline: 1.0491x; 1.0028x over previous
.LBB1_8:
	s_lshl_b32 s12, s62, 9
	v_lshl_add_u64 v[6:7], s[12:13], 4, v[210:211]
	v_add_co_u32_e32 v34, vcc, s52, v6
	s_mov_b32 s12, s13
	s_nop 0
	v_addc_co_u32_e32 v35, vcc, 0, v7, vcc
	global_load_dwordx4 v[2:5], v[34:35], off offset:-4096
	v_add_co_u32_e32 v36, vcc, s49, v6
	s_xor_b64 s[50:51], s[14:15], -1
	s_nop 0
	v_addc_co_u32_e32 v37, vcc, 0, v7, vcc
	global_load_dwordx4 v[6:9], v[36:37], off offset:1024
	global_load_dwordx4 v[10:13], v[36:37], off offset:2048
	global_load_dwordx4 v[14:17], v[34:35], off
	s_mov_b32 s14, s13
	s_mov_b32 s15, s13
	s_mov_b32 s16, s13
	s_mov_b32 s17, s13
	s_mov_b32 s18, s13
	s_mov_b32 s19, s13
	s_mov_b32 s20, s13
	s_mov_b32 s21, s13
	s_mov_b32 s22, s13
	s_mov_b32 s23, s13
	s_mov_b32 s24, s13
	s_mov_b32 s25, s13
	s_mov_b32 s26, s13
	s_mov_b32 s27, s13
	s_waitcnt vmcnt(3) lgkmcnt(7)
	v_mfma_f32_32x32x16_f16 v[18:33], v[2:5], v[146:149], 0
	global_load_dwordx4 v[2:5], v[36:37], off offset:3072
	s_waitcnt vmcnt(3) lgkmcnt(6)
	v_mfma_f32_32x32x16_f16 v[18:33], v[6:9], v[150:153], v[18:33]
	global_load_dwordx4 v[6:9], v[34:35], off offset:1024
	s_waitcnt vmcnt(3) lgkmcnt(5)
	v_mfma_f32_32x32x16_f16 v[18:33], v[10:13], v[154:157], v[18:33]
	global_load_dwordx4 v[10:13], v[34:35], off offset:2048
	s_nop 0
	global_load_dwordx4 v[34:37], v[34:35], off offset:3072
	s_waitcnt vmcnt(3) lgkmcnt(4)
	v_mfma_f32_32x32x16_f16 v[18:33], v[2:5], v[158:161], v[18:33]
	s_waitcnt lgkmcnt(3)
	v_mfma_f32_32x32x16_f16 v[18:33], v[14:17], v[162:165], v[18:33]
	s_waitcnt vmcnt(2) lgkmcnt(2)
	v_mfma_f32_32x32x16_f16 v[18:33], v[6:9], v[166:169], v[18:33]
	s_waitcnt vmcnt(1) lgkmcnt(1)
	v_mfma_f32_32x32x16_f16 v[18:33], v[10:13], v[170:173], v[18:33]
	v_mov_b64_e32 v[2:3], s[12:13]
	v_mov_b64_e32 v[4:5], s[14:15]
	v_mov_b64_e32 v[6:7], s[16:17]
	v_mov_b64_e32 v[8:9], s[18:19]
	v_mov_b64_e32 v[10:11], s[20:21]
	v_mov_b64_e32 v[12:13], s[22:23]
	v_mov_b64_e32 v[14:15], s[24:25]
	s_waitcnt vmcnt(0) lgkmcnt(0)
	v_mfma_f32_32x32x16_f16 v[18:33], v[34:37], v[174:177], v[18:33]
	v_mov_b64_e32 v[16:17], s[26:27]
	s_mul_i32 s12, s62, 20
	s_lshl_b64 s[14:15], s[12:13], 2
	s_add_u32 s14, s10, s14
	s_addc_u32 s15, s11, s15
	s_load_dwordx16 s[16:31], s[14:15], 0x0
	s_load_dwordx4 s[40:43], s[14:15], 0x40
	s_mul_i32 s12, s62, 0x1b0000
	s_nop 3
	ds_bpermute_b32 v34, v225, v18
	ds_bpermute_b32 v35, v225, v19
	ds_bpermute_b32 v36, v225, v20
	ds_bpermute_b32 v37, v225, v21
	ds_bpermute_b32 v38, v225, v22
	ds_bpermute_b32 v39, v225, v23
	ds_bpermute_b32 v40, v225, v24
	ds_bpermute_b32 v41, v225, v25
	ds_bpermute_b32 v42, v225, v26
	ds_bpermute_b32 v43, v225, v27
	ds_bpermute_b32 v44, v225, v28
	ds_bpermute_b32 v45, v225, v29
	ds_bpermute_b32 v46, v225, v30
	ds_bpermute_b32 v47, v225, v31
	ds_bpermute_b32 v48, v225, v32
	ds_bpermute_b32 v49, v225, v33
	s_waitcnt lgkmcnt(0)
	v_cndmask_b32_e64 v50, v34, v18, s[0:1]
	v_cndmask_b32_e64 v19, v35, v19, s[0:1]
	v_cndmask_b32_e64 v20, v36, v20, s[0:1]
	v_cndmask_b32_e64 v21, v37, v21, s[0:1]
	v_cndmask_b32_e64 v18, v18, v34, s[0:1]
	v_cndmask_b32_e64 v34, v38, v22, s[0:1]
	v_cndmask_b32_e64 v23, v39, v23, s[0:1]
	v_cndmask_b32_e64 v24, v40, v24, s[0:1]
	v_cndmask_b32_e64 v25, v41, v25, s[0:1]
	v_cndmask_b32_e64 v22, v22, v38, s[0:1]
	v_add_f32_e32 v37, s16, v50
	v_add_f32_e32 v19, s17, v19
	v_add_f32_e32 v20, s18, v20
	v_add_f32_e32 v21, s19, v21
	v_add_f32_e32 v34, s21, v34
	v_add_f32_e32 v23, s22, v23
	v_add_f32_e32 v24, s23, v24
	v_add_f32_e32 v25, s24, v25
	v_cndmask_b32_e64 v35, v42, v26, s[0:1]
	v_cndmask_b32_e64 v27, v43, v27, s[0:1]
	v_cndmask_b32_e64 v28, v44, v28, s[0:1]
	v_cndmask_b32_e64 v29, v45, v29, s[0:1]
	v_add_f32_e32 v18, s20, v18
	v_add_f32_e32 v22, s25, v22
	v_max_f32_e32 v38, v37, v19
	v_max_f32_e32 v39, v20, v21
	v_max_f32_e32 v40, v34, v23
	v_max_f32_e32 v41, v24, v25
	v_cndmask_b32_e64 v26, v26, v42, s[0:1]
	v_cndmask_b32_e64 v36, v46, v30, s[0:1]
	v_cndmask_b32_e64 v31, v47, v31, s[0:1]
	v_cndmask_b32_e64 v32, v48, v32, s[0:1]
	v_add_f32_e32 v35, s26, v35
	v_add_f32_e32 v27, s27, v27
	v_add_f32_e32 v28, s28, v28
	v_add_f32_e32 v29, s29, v29
	v_max3_f32 v38, v38, v39, v18
	v_max3_f32 v39, v40, v41, v22
	v_cndmask_b32_e64 v33, v49, v33, s[0:1]
	v_add_f32_e32 v26, s30, v26
	v_add_f32_e32 v36, s31, v36
	v_add_f32_e32 v31, s40, v31
	v_add_f32_e32 v32, s41, v32
	v_max_f32_e32 v42, v35, v27
	v_max_f32_e32 v43, v28, v29
	v_sub_f32_e32 v34, v34, v39
	v_add_f32_e32 v33, s42, v33
	v_cndmask_b32_e64 v30, v30, v46, s[0:1]
	v_max3_f32 v40, v42, v43, v26
	v_sub_f32_e32 v37, v37, v38
	v_sub_f32_e32 v23, v23, v39
	v_mul_f32_e32 v34, 0x3fb8aa3b, v34
	v_add_f32_e32 v30, s43, v30
	v_max_f32_e32 v41, v36, v31
	v_max_f32_e32 v42, v32, v33
	v_sub_f32_e32 v19, v19, v38
	v_sub_f32_e32 v24, v24, v39
	v_sub_f32_e32 v35, v35, v40
	v_mul_f32_e32 v37, 0x3fb8aa3b, v37
	v_mul_f32_e32 v23, 0x3fb8aa3b, v23
	v_exp_f32_e32 v34, v34
	v_max3_f32 v41, v41, v42, v30
	v_sub_f32_e32 v20, v20, v38
	v_sub_f32_e32 v25, v25, v39
	v_sub_f32_e32 v27, v27, v40
	v_mul_f32_e32 v19, 0x3fb8aa3b, v19
	v_mul_f32_e32 v24, 0x3fb8aa3b, v24
	v_mul_f32_e32 v35, 0x3fb8aa3b, v35
	v_exp_f32_e32 v37, v37
	v_exp_f32_e32 v23, v23
	v_sub_f32_e32 v36, v36, v41
	v_sub_f32_e32 v21, v21, v38
	v_sub_f32_e32 v22, v22, v39
	v_sub_f32_e32 v28, v28, v40
	v_mul_f32_e32 v20, 0x3fb8aa3b, v20
	v_mul_f32_e32 v25, 0x3fb8aa3b, v25
	v_mul_f32_e32 v27, 0x3fb8aa3b, v27
	v_exp_f32_e32 v19, v19
	v_exp_f32_e32 v24, v24
	v_exp_f32_e32 v35, v35
	v_mul_f32_e32 v36, 0x3fb8aa3b, v36
	v_sub_f32_e32 v31, v31, v41
	v_sub_f32_e32 v18, v18, v38
	v_sub_f32_e32 v29, v29, v40
	v_mul_f32_e32 v21, 0x3fb8aa3b, v21
	v_mul_f32_e32 v22, 0x3fb8aa3b, v22
	v_mul_f32_e32 v28, 0x3fb8aa3b, v28
	v_exp_f32_e32 v20, v20
	v_exp_f32_e32 v25, v25
	v_exp_f32_e32 v27, v27
	v_exp_f32_e32 v36, v36
	v_mul_f32_e32 v31, 0x3fb8aa3b, v31
	v_sub_f32_e32 v32, v32, v41
	v_sub_f32_e32 v26, v26, v40
	v_mul_f32_e32 v18, 0x3fb8aa3b, v18
	v_mul_f32_e32 v29, 0x3fb8aa3b, v29
	v_exp_f32_e32 v21, v21
	v_exp_f32_e32 v22, v22
	v_exp_f32_e32 v28, v28
	v_add_f32_e32 v39, 0, v34
	v_exp_f32_e32 v31, v31
	v_mul_f32_e32 v32, 0x3fb8aa3b, v32
	v_sub_f32_e32 v33, v33, v41
	v_mul_f32_e32 v26, 0x3fb8aa3b, v26
	v_exp_f32_e32 v18, v18
	v_exp_f32_e32 v29, v29
	v_add_f32_e32 v38, 0, v37
	v_add_f32_e32 v39, v23, v39
	v_exp_f32_e32 v32, v32
	v_mul_f32_e32 v33, 0x3fb8aa3b, v33
	v_sub_f32_e32 v30, v30, v41
	v_exp_f32_e32 v26, v26
	v_add_f32_e32 v40, 0, v35
	v_add_f32_e32 v38, v19, v38
	v_add_f32_e32 v39, v24, v39
	v_exp_f32_e32 v33, v33
	v_mul_f32_e32 v30, 0x3fb8aa3b, v30
	v_add_f32_e32 v40, v27, v40
	v_add_f32_e32 v38, v20, v38
	v_add_f32_e32 v39, v25, v39
	v_add_f32_e32 v42, 0, v36
	v_exp_f32_e32 v30, v30
	v_add_f32_e32 v38, v21, v38
	v_add_f32_e32 v39, v22, v39
	v_add_f32_e32 v40, v28, v40
	v_add_f32_e32 v41, v31, v42
	v_add_f32_e32 v38, v18, v38
	v_rcp_f32_e32 v39, v39
	v_add_f32_e32 v40, v29, v40
	v_add_f32_e32 v41, v32, v41
	v_rcp_f32_e32 v38, v38
	v_add_f32_e32 v40, v26, v40
	v_add_f32_e32 v41, v33, v41
	v_rcp_f32_e32 v40, v40
	v_add_f32_e32 v41, v30, v41
	v_rcp_f32_e32 v41, v41
	v_mul_f32_e32 v34, v34, v39
	v_mul_f32_e32 v23, v23, v39
	v_fmac_f32_e32 v34, v37, v38
	v_fmac_f32_e32 v23, v19, v38
	v_mul_f32_e32 v24, v24, v39
	v_fmac_f32_e32 v34, v35, v40
	v_fmac_f32_e32 v23, v27, v40
	v_mul_f32_e32 v22, v22, v39
	v_mul_f32_e32 v29, v29, v40
	v_fmac_f32_e32 v34, v36, v41
	v_fmac_f32_e32 v23, v31, v41
	v_fmac_f32_e32 v24, v20, v38
	v_fmac_f32_e32 v24, v28, v40
	v_cndmask_b32_e64 v20, v22, v34, s[4:5]
	v_cndmask_b32_e64 v22, v29, v23, s[4:5]
	v_mul_f32_e32 v21, v21, v38
	v_mul_f32_e32 v18, v18, v38
	v_mul_f32_e32 v25, v25, v39
	v_mul_f32_e32 v26, v26, v40
	v_mul_f32_e32 v33, v33, v41
	v_mul_f32_e32 v30, v30, v41
	v_fmac_f32_e32 v24, v32, v41
	v_mul_f32_e32 v20, 0x3e800000, v20
	v_mul_f32_e32 v22, 0x3e800000, v22
	v_mul_f32_e32 v19, 0x3e800000, v25
	ds_write2st64_b32 v222, v20, v22 offset1:8
	v_cndmask_b32_e64 v20, v26, v24, s[4:5]
	v_cndmask_b32_e64 v21, v33, v21, s[4:5]
	v_cndmask_b32_e64 v18, v30, v18, s[4:5]
	v_mul_f32_e32 v20, 0x3e800000, v20
	v_mul_f32_e32 v21, 0x3e800000, v21
	v_mul_f32_e32 v18, 0x3e800000, v18
	v_cndmask_b32_e64 v19, 0, v19, s[4:5]
	ds_write2st64_b32 v222, v20, v21 offset0:16 offset1:24
	ds_write2st64_b32 v222, v18, v19 offset0:32 offset1:40
	s_mul_hi_u32 s14, s62, 0x1b0000
	s_add_u32 s12, s44, s12
	v_mov_b64_e32 v[64:65], v[16:17]
	v_mov_b64_e32 v[48:49], v[16:17]
	v_mov_b64_e32 v[32:33], v[16:17]
	s_addc_u32 s16, s45, s14
	s_mov_b32 s17, 0
	v_mov_b64_e32 v[62:63], v[14:15]
	v_mov_b64_e32 v[60:61], v[12:13]
	v_mov_b64_e32 v[58:59], v[10:11]
	v_mov_b64_e32 v[56:57], v[8:9]
	v_mov_b64_e32 v[54:55], v[6:7]
	v_mov_b64_e32 v[52:53], v[4:5]
	v_mov_b64_e32 v[50:51], v[2:3]
	v_mov_b64_e32 v[46:47], v[14:15]
	v_mov_b64_e32 v[44:45], v[12:13]
	v_mov_b64_e32 v[42:43], v[10:11]
	v_mov_b64_e32 v[40:41], v[8:9]
	v_mov_b64_e32 v[38:39], v[6:7]
	v_mov_b64_e32 v[36:37], v[4:5]
	v_mov_b64_e32 v[34:35], v[2:3]
	v_mov_b64_e32 v[30:31], v[14:15]
	v_mov_b64_e32 v[28:29], v[12:13]
	v_mov_b64_e32 v[26:27], v[10:11]
	v_mov_b64_e32 v[24:25], v[8:9]
	v_mov_b64_e32 v[22:23], v[6:7]
	v_mov_b64_e32 v[20:21], v[4:5]
	v_mov_b64_e32 v[18:19], v[2:3]
	s_mov_b32 s18, 0
	s_mul_i32 s25, s33, 0x9000
	s_add_i32 s26, s33, -1
	s_cmp_eq_u32 s33, 0
	s_cselect_b32 s26, 2, s26
	s_mul_i32 s26, s26, 0x9000
	s_cmp_lg_u32 s4, 0
	s_cselect_b32 s27, 0x7fffffff, 40
	v_readfirstlane_b32 s28, v0
	s_lshl_b32 s28, s28, 4
	s_and_b32 s29, s28, 0xfffff000
	s_and_b32 s28, s28, 0xfffffc00
	s_add_i32 s28, s28, 0x8000
	s_sub_i32 s29, 0x8000, s29
	s_add_i32 s22, s25, 0x8000
	v_add_u32_e32 v189, s22, v246
	v_add_u32_e32 v248, s25, v247
	ds_read_b128 v[130:133], v189 offset:32768
	ds_read_b128 v[134:137], v189 offset:32800
	ds_read_b128 v[138:141], v189 offset:32832
	ds_read_b128 v[142:145], v189 offset:32864
	ds_read_b128 v[190:193], v248 offset:32768
	ds_read_b128 v[194:197], v248 offset:33792
	ds_read_b128 v[198:201], v248 offset:34816
	ds_read_b128 v[202:205], v248 offset:35840
	ds_read_b128 v[212:215], v248 offset:36864
	ds_read_b128 v[228:231], v248 offset:37888
	ds_read_b128 v[232:235], v248 offset:38912
	ds_read_b128 v[236:239], v248 offset:39936
	s_branch .LBB1_10

.Lnf_9b:
	s_mov_b32 s26, s25
	s_add_i32 s25, s25, 0x9000
	s_cmp_lg_u32 s26, 0x12000
	s_cselect_b32 s25, s25, 0
	s_add_i32 s22, s25, 0x8000
	v_add_u32_e32 v189, s22, v246
	v_add_u32_e32 v248, s25, v247
	ds_read_b128 v[130:133], v189 offset:32768
	ds_read_b128 v[134:137], v189 offset:32800
	ds_read_b128 v[138:141], v189 offset:32832
	ds_read_b128 v[142:145], v189 offset:32864
	ds_read_b128 v[190:193], v248 offset:32768
	ds_read_b128 v[194:197], v248 offset:33792
	ds_read_b128 v[198:201], v248 offset:34816
	ds_read_b128 v[202:205], v248 offset:35840
	ds_read_b128 v[212:215], v248 offset:36864
	ds_read_b128 v[228:231], v248 offset:37888
	ds_read_b128 v[232:235], v248 offset:38912
	ds_read_b128 v[236:239], v248 offset:39936
	s_add_i32 s18, s18, 1
	s_add_u32 s12, s12, 0x9000
	s_addc_u32 s16, s16, 0
	s_cmp_eq_u32 s18, 48
	s_waitcnt vmcnt(0) lgkmcnt(12)
	s_barrier
	s_cbranch_scc1 .LBB1_19
.LBB1_10:
	s_cmp_ge_u32 s18, s27
	s_cbranch_scc1 .Lnf_inact
	s_and_b32 s19, s18, 7
	s_cmp_lg_u32 s19, 0
	s_cbranch_scc1 .LBB1_15
	ds_read_b128 v[66:69], v189 offset:33280
	ds_read_b128 v[70:73], v189 offset:33312
	ds_read_b128 v[74:77], v189 offset:33344
	ds_read_b128 v[78:81], v189 offset:33376
	ds_read_b128 v[82:85], v189 offset:33408
	ds_read_b128 v[86:89], v189 offset:33440
	ds_read_b128 v[90:93], v189 offset:33472
	ds_read_b128 v[94:97], v189 offset:33504
	ds_read_b128 v[98:101], v189 offset:33536
	ds_read_b128 v[102:105], v189 offset:33568
	ds_read_b128 v[106:109], v189 offset:33600
	ds_read_b128 v[110:113], v189 offset:33632
	ds_read_b128 v[114:117], v189 offset:33664
	ds_read_b128 v[118:121], v189 offset:33696
	ds_read_b128 v[122:125], v189 offset:33728
	ds_read_b128 v[126:129], v189 offset:33760
	s_waitcnt lgkmcnt(12)
	v_mfma_f32_32x32x16_f16 v[66:81], v[178:181], v[146:149], v[66:81]
	s_waitcnt lgkmcnt(8)
	v_mfma_f32_32x32x16_f16 v[82:97], v[178:181], v[154:157], v[82:97]
	s_waitcnt lgkmcnt(4)
	v_mfma_f32_32x32x16_f16 v[98:113], v[178:181], v[162:165], v[98:113]
	s_waitcnt lgkmcnt(0)
	v_mfma_f32_32x32x16_f16 v[114:129], v[178:181], v[170:173], v[114:129]
	v_mfma_f32_32x32x16_f16 v[66:81], v[182:185], v[150:153], v[66:81]
	v_mfma_f32_32x32x16_f16 v[82:97], v[182:185], v[158:161], v[82:97]
	v_mfma_f32_32x32x16_f16 v[98:113], v[182:185], v[166:169], v[98:113]
	v_mfma_f32_32x32x16_f16 v[114:129], v[182:185], v[174:177], v[114:129]
.LBB1_15:
	s_waitcnt lgkmcnt(0)
	v_mfma_f32_32x32x16_f16 v[130:145], v[190:193], v[146:149], v[130:145]
	v_mfma_f32_32x32x16_f16 v[130:145], v[194:197], v[150:153], v[130:145]
	v_mfma_f32_32x32x16_f16 v[130:145], v[198:201], v[154:157], v[130:145]
	v_mfma_f32_32x32x16_f16 v[130:145], v[202:205], v[158:161], v[130:145]
	s_add_i32 s23, s26, s28
	s_add_i32 m0, s23, 0x0
	s_add_u32 s20, s12, 0x12000
	s_addc_u32 s21, s16, 0
	global_load_lds_dwordx4 v226, s[20:21]
	v_mfma_f32_32x32x16_f16 v[130:145], v[212:215], v[162:165], v[130:145]
	s_add_i32 m0, s23, 0x2000
	s_add_u32 s20, s12, 0x14000
	s_addc_u32 s21, s16, 0
	global_load_lds_dwordx4 v226, s[20:21]
	v_mfma_f32_32x32x16_f16 v[130:145], v[228:231], v[166:169], v[130:145]
	s_add_i32 m0, s23, 0x4000
	s_add_u32 s20, s12, 0x16000
	s_addc_u32 s21, s16, 0
	global_load_lds_dwordx4 v226, s[20:21]
	v_mfma_f32_32x32x16_f16 v[130:145], v[232:235], v[170:173], v[130:145]
	s_add_i32 m0, s23, 0x6000
	s_add_u32 s20, s12, 0x18000
	s_addc_u32 s21, s16, 0
	global_load_lds_dwordx4 v226, s[20:21]
	v_mfma_f32_32x32x16_f16 v[130:145], v[236:239], v[174:177], v[130:145]
	s_add_i32 m0, s23, s29
	s_add_u32 s20, s12, 0x1a000
	s_addc_u32 s21, s16, 0
	global_load_lds_dwordx4 v224, s[20:21]
	ds_read_b128 v[190:193], v248 offset:40960
	ds_read_b128 v[194:197], v248 offset:41984
	ds_read_b128 v[198:201], v248 offset:43008
	ds_read_b128 v[202:205], v248 offset:44032
	ds_read_b128 v[212:215], v248 offset:45056
	ds_read_b128 v[228:231], v248 offset:46080
	ds_read_b128 v[232:235], v248 offset:47104
	ds_read_b128 v[236:239], v248 offset:48128
	v_cvt_pk_f16_f32 v130, v130, v131
	v_cvt_pk_f16_f32 v131, v132, v133
	v_cvt_pk_f16_f32 v132, v134, v135
	v_cvt_pk_f16_f32 v133, v136, v137
	v_and_b32_e32 v134, 0x7fff7fff, v130
	v_and_b32_e32 v135, 0x7fff7fff, v131
	v_and_b32_e32 v136, 0x7fff7fff, v132
	v_and_b32_e32 v137, 0x7fff7fff, v133
	v_pk_min_f16 v134, v134, v186
	v_pk_min_f16 v135, v135, v186
	v_pk_min_f16 v136, v136, v186
	v_pk_min_f16 v137, v137, v186
	v_pk_max_f16 v130, v130, v187
	v_pk_max_f16 v131, v131, v187
	s_nop 0
	v_pk_fma_f16 v134, v134, s53, -1.0 op_sel_hi:[1,0,0]
	v_pk_fma_f16 v135, v135, s53, -1.0 op_sel_hi:[1,0,0]
	v_pk_fma_f16 v136, v136, s53, -1.0 op_sel_hi:[1,0,0]
	v_pk_fma_f16 v137, v137, s53, -1.0 op_sel_hi:[1,0,0]
	v_pk_fma_f16 v240, v134, s54, v188 op_sel_hi:[1,0,0]
	v_pk_fma_f16 v241, v135, s54, v188 op_sel_hi:[1,0,0]
	v_pk_fma_f16 v242, v136, s54, v188 op_sel_hi:[1,0,0]
	v_pk_fma_f16 v243, v137, s54, v188 op_sel_hi:[1,0,0]
	v_pk_fma_f16 v240, v134, v240, s55 op_sel_hi:[1,1,0]
	v_pk_fma_f16 v241, v135, v241, s55 op_sel_hi:[1,1,0]
	v_pk_fma_f16 v242, v136, v242, s55 op_sel_hi:[1,1,0]
	v_pk_fma_f16 v243, v137, v243, s55 op_sel_hi:[1,1,0]
	v_pk_fma_f16 v240, v134, v240, s56 op_sel_hi:[1,1,0]
	v_pk_fma_f16 v241, v135, v241, s56 op_sel_hi:[1,1,0]
	v_pk_fma_f16 v242, v136, v242, s56 op_sel_hi:[1,1,0]
	v_pk_fma_f16 v243, v137, v243, s56 op_sel_hi:[1,1,0]
	v_pk_fma_f16 v240, v134, v240, s57 op_sel_hi:[1,1,0]
	v_pk_fma_f16 v241, v135, v241, s57 op_sel_hi:[1,1,0]
	v_pk_fma_f16 v242, v136, v242, s57 op_sel_hi:[1,1,0]
	v_pk_fma_f16 v243, v137, v243, s57 op_sel_hi:[1,1,0]
	v_pk_fma_f16 v240, v134, v240, s58 op_sel_hi:[1,1,0]
	v_pk_fma_f16 v241, v135, v241, s58 op_sel_hi:[1,1,0]
	v_pk_fma_f16 v242, v136, v242, s58 op_sel_hi:[1,1,0]
	v_pk_fma_f16 v243, v137, v243, s58 op_sel_hi:[1,1,0]
	v_pk_fma_f16 v240, v134, v240, s59 op_sel_hi:[1,1,0]
	v_pk_fma_f16 v241, v135, v241, s59 op_sel_hi:[1,1,0]
	v_pk_fma_f16 v242, v136, v242, s59 op_sel_hi:[1,1,0]
	v_pk_fma_f16 v243, v137, v243, s59 op_sel_hi:[1,1,0]
	v_pk_max_f16 v132, v132, v187
	v_pk_max_f16 v133, v133, v187
	v_pk_fma_f16 v134, v134, v240, s60 op_sel_hi:[1,1,0]
	v_pk_fma_f16 v135, v135, v241, s60 op_sel_hi:[1,1,0]
	v_pk_fma_f16 v136, v136, v242, s60 op_sel_hi:[1,1,0]
	v_pk_fma_f16 v137, v137, v243, s60 op_sel_hi:[1,1,0]
	v_pk_add_f16 v130, v130, v134
	v_pk_add_f16 v131, v131, v135
	v_pk_add_f16 v132, v132, v136
	v_pk_add_f16 v133, v133, v137
	v_cvt_pk_f16_f32 v134, v138, v139
	v_cvt_pk_f16_f32 v135, v140, v141
	v_cvt_pk_f16_f32 v136, v142, v143
	v_cvt_pk_f16_f32 v137, v144, v145
	v_and_b32_e32 v138, 0x7fff7fff, v134
	v_and_b32_e32 v139, 0x7fff7fff, v135
	v_and_b32_e32 v140, 0x7fff7fff, v136
	v_and_b32_e32 v141, 0x7fff7fff, v137
	v_pk_min_f16 v138, v138, v186
	v_pk_min_f16 v139, v139, v186
	v_pk_min_f16 v140, v140, v186
	v_pk_min_f16 v141, v141, v186
	s_waitcnt lgkmcnt(0)
	v_mfma_f32_32x32x16_f16 v[66:81], v[190:193], v[130:133], v[66:81]
	v_pk_fma_f16 v138, v138, s53, -1.0 op_sel_hi:[1,0,0]
	v_pk_fma_f16 v139, v139, s53, -1.0 op_sel_hi:[1,0,0]
	v_pk_fma_f16 v140, v140, s53, -1.0 op_sel_hi:[1,0,0]
	v_pk_fma_f16 v141, v141, s53, -1.0 op_sel_hi:[1,0,0]
	v_pk_fma_f16 v142, v138, s54, v188 op_sel_hi:[1,0,0]
	v_pk_fma_f16 v143, v139, s54, v188 op_sel_hi:[1,0,0]
	v_pk_fma_f16 v144, v140, s54, v188 op_sel_hi:[1,0,0]
	v_pk_fma_f16 v145, v141, s54, v188 op_sel_hi:[1,0,0]
	v_mfma_f32_32x32x16_f16 v[82:97], v[198:201], v[130:133], v[82:97]
	v_pk_fma_f16 v142, v138, v142, s55 op_sel_hi:[1,1,0]
	v_pk_fma_f16 v143, v139, v143, s55 op_sel_hi:[1,1,0]
	v_pk_fma_f16 v144, v140, v144, s55 op_sel_hi:[1,1,0]
	v_pk_fma_f16 v145, v141, v145, s55 op_sel_hi:[1,1,0]
	v_pk_fma_f16 v142, v138, v142, s56 op_sel_hi:[1,1,0]
	v_pk_fma_f16 v143, v139, v143, s56 op_sel_hi:[1,1,0]
	v_pk_fma_f16 v144, v140, v144, s56 op_sel_hi:[1,1,0]
	v_mfma_f32_32x32x16_f16 v[98:113], v[212:215], v[130:133], v[98:113]
	v_pk_fma_f16 v145, v141, v145, s56 op_sel_hi:[1,1,0]
	v_pk_fma_f16 v142, v138, v142, s57 op_sel_hi:[1,1,0]
	v_pk_fma_f16 v143, v139, v143, s57 op_sel_hi:[1,1,0]
	v_pk_fma_f16 v144, v140, v144, s57 op_sel_hi:[1,1,0]
	v_pk_fma_f16 v145, v141, v145, s57 op_sel_hi:[1,1,0]
	v_pk_fma_f16 v142, v138, v142, s58 op_sel_hi:[1,1,0]
	v_pk_fma_f16 v143, v139, v143, s58 op_sel_hi:[1,1,0]
	v_mfma_f32_32x32x16_f16 v[114:129], v[232:235], v[130:133], v[114:129]
	v_pk_fma_f16 v144, v140, v144, s58 op_sel_hi:[1,1,0]
	v_pk_fma_f16 v145, v141, v145, s58 op_sel_hi:[1,1,0]
	v_pk_fma_f16 v142, v138, v142, s59 op_sel_hi:[1,1,0]
	v_pk_fma_f16 v143, v139, v143, s59 op_sel_hi:[1,1,0]
	v_pk_fma_f16 v144, v140, v144, s59 op_sel_hi:[1,1,0]
	v_pk_fma_f16 v145, v141, v145, s59 op_sel_hi:[1,1,0]
	v_pk_max_f16 v134, v134, v187
	v_pk_max_f16 v135, v135, v187
	v_pk_max_f16 v136, v136, v187
	v_pk_max_f16 v137, v137, v187
	v_pk_fma_f16 v138, v138, v142, s60 op_sel_hi:[1,1,0]
	v_pk_fma_f16 v139, v139, v143, s60 op_sel_hi:[1,1,0]
	v_pk_fma_f16 v140, v140, v144, s60 op_sel_hi:[1,1,0]
	v_pk_fma_f16 v141, v141, v145, s60 op_sel_hi:[1,1,0]
	v_pk_add_f16 v134, v134, v138
	v_pk_add_f16 v135, v135, v139
	v_pk_add_f16 v136, v136, v140
	v_pk_add_f16 v137, v137, v141
	s_cmp_lg_u32 s19, 7
	s_nop 0
	v_mfma_f32_32x32x16_f16 v[66:81], v[194:197], v[134:137], v[66:81]
	v_mfma_f32_32x32x16_f16 v[82:97], v[202:205], v[134:137], v[82:97]
	v_mfma_f32_32x32x16_f16 v[98:113], v[228:231], v[134:137], v[98:113]
	v_mfma_f32_32x32x16_f16 v[114:129], v[236:239], v[134:137], v[114:129]
	s_cbranch_scc1 .LBB1_17
	ds_read_b128 v[132:135], v189 offset:33312
	ds_read_b128 v[136:139], v189 offset:33344
	ds_read_b128 v[140:143], v189 offset:33824
	ds_read_b128 v[190:193], v189 offset:33856
	ds_read_b128 v[194:197], v189 offset:33792
	ds_read_b128 v[198:201], v189 offset:33376
	ds_read_b128 v[202:205], v189 offset:33888
	s_lshl_b32 s19, s18, 6
	s_and_b32 s19, s19, 0xe00
	v_lshl_add_u32 v130, s19, 2, v222
	ds_read_b128 v[212:215], v189 offset:33280
	ds_read_b32 v130, v130
	v_pk_add_f32 v[144:145], v[66:67], v[68:69]
	v_pk_mul_f32 v[228:229], v[66:67], v[66:67]
	v_pk_add_f32 v[230:231], v[82:83], v[84:85]
	v_pk_mul_f32 v[232:233], v[82:83], v[82:83]
	v_pk_add_f32 v[234:235], v[98:99], v[100:101]
	v_pk_mul_f32 v[236:237], v[98:99], v[98:99]
	v_pk_add_f32 v[238:239], v[114:115], v[116:117]
	v_pk_mul_f32 v[240:241], v[114:115], v[114:115]
	v_pk_fma_f32 v[228:229], v[68:69], v[68:69], v[228:229]
	v_pk_fma_f32 v[232:233], v[84:85], v[84:85], v[232:233]
	v_pk_fma_f32 v[236:237], v[100:101], v[100:101], v[236:237]
	v_pk_fma_f32 v[240:241], v[116:117], v[116:117], v[240:241]
	v_pk_add_f32 v[144:145], v[70:71], v[144:145]
	v_pk_add_f32 v[230:231], v[86:87], v[230:231]
	v_pk_add_f32 v[234:235], v[102:103], v[234:235]
	v_pk_add_f32 v[238:239], v[118:119], v[238:239]
	v_pk_fma_f32 v[228:229], v[70:71], v[70:71], v[228:229]
	v_pk_fma_f32 v[232:233], v[86:87], v[86:87], v[232:233]
	v_pk_fma_f32 v[236:237], v[102:103], v[102:103], v[236:237]
	v_pk_fma_f32 v[240:241], v[118:119], v[118:119], v[240:241]
	v_pk_add_f32 v[144:145], v[72:73], v[144:145]
	v_pk_add_f32 v[230:231], v[88:89], v[230:231]
	v_pk_add_f32 v[234:235], v[104:105], v[234:235]
	v_pk_add_f32 v[238:239], v[120:121], v[238:239]
	v_pk_fma_f32 v[228:229], v[72:73], v[72:73], v[228:229]
	v_pk_fma_f32 v[232:233], v[88:89], v[88:89], v[232:233]
	v_pk_fma_f32 v[236:237], v[104:105], v[104:105], v[236:237]
	v_pk_fma_f32 v[240:241], v[120:121], v[120:121], v[240:241]
	v_pk_add_f32 v[144:145], v[74:75], v[144:145]
	v_pk_add_f32 v[230:231], v[90:91], v[230:231]
	v_pk_add_f32 v[234:235], v[106:107], v[234:235]
	v_pk_add_f32 v[238:239], v[122:123], v[238:239]
	v_pk_fma_f32 v[228:229], v[74:75], v[74:75], v[228:229]
	v_pk_fma_f32 v[232:233], v[90:91], v[90:91], v[232:233]
	v_pk_fma_f32 v[236:237], v[106:107], v[106:107], v[236:237]
	v_pk_fma_f32 v[240:241], v[122:123], v[122:123], v[240:241]
	v_pk_add_f32 v[144:145], v[76:77], v[144:145]
	v_pk_add_f32 v[230:231], v[92:93], v[230:231]
	v_pk_add_f32 v[234:235], v[108:109], v[234:235]
	v_pk_add_f32 v[238:239], v[124:125], v[238:239]
	v_pk_fma_f32 v[228:229], v[76:77], v[76:77], v[228:229]
	v_pk_fma_f32 v[232:233], v[92:93], v[92:93], v[232:233]
	v_pk_fma_f32 v[236:237], v[108:109], v[108:109], v[236:237]
	v_pk_fma_f32 v[240:241], v[124:125], v[124:125], v[240:241]
	v_pk_add_f32 v[144:145], v[78:79], v[144:145]
	v_pk_add_f32 v[230:231], v[94:95], v[230:231]
	v_pk_add_f32 v[234:235], v[110:111], v[234:235]
	v_pk_add_f32 v[238:239], v[126:127], v[238:239]
	v_pk_fma_f32 v[228:229], v[78:79], v[78:79], v[228:229]
	v_pk_fma_f32 v[232:233], v[94:95], v[94:95], v[232:233]
	v_pk_fma_f32 v[236:237], v[110:111], v[110:111], v[236:237]
	v_pk_fma_f32 v[240:241], v[126:127], v[126:127], v[240:241]
	v_pk_add_f32 v[144:145], v[80:81], v[144:145]
	v_pk_add_f32 v[230:231], v[96:97], v[230:231]
	v_pk_add_f32 v[234:235], v[112:113], v[234:235]
	v_pk_add_f32 v[238:239], v[128:129], v[238:239]
	v_pk_fma_f32 v[228:229], v[80:81], v[80:81], v[228:229]
	v_pk_fma_f32 v[232:233], v[96:97], v[96:97], v[232:233]
	v_pk_fma_f32 v[236:237], v[112:113], v[112:113], v[236:237]
	v_pk_fma_f32 v[240:241], v[128:129], v[128:129], v[240:241]
	v_pk_add_f32 v[144:145], v[144:145], v[230:231]
	v_pk_add_f32 v[230:231], v[234:235], v[238:239]
	v_pk_add_f32 v[228:229], v[228:229], v[232:233]
	v_pk_add_f32 v[144:145], v[144:145], v[230:231]
	v_pk_add_f32 v[230:231], v[236:237], v[240:241]
	s_nop 0
	v_pk_add_f32 v[228:229], v[228:229], v[230:231]
	v_mov_b32_e32 v231, v144
	v_mov_b32_e32 v230, v228
	v_mov_b32_e32 v144, v229
	v_pk_add_f32 v[144:145], v[230:231], v[144:145]
	ds_bpermute_b32 v229, v225, v145
	ds_bpermute_b32 v228, v225, v144
	s_waitcnt lgkmcnt(0)
	v_pk_add_f32 v[144:145], v[144:145], v[228:229]
	s_nop 0
	v_pk_mul_f32 v[144:145], v[144:145], s[48:49] op_sel_hi:[1,0]
	s_nop 0
	v_fma_f32 v131, -v145, v145, v144
	v_add_f32_e32 v131, 0x3727c5ac, v131
	v_mul_f32_e32 v144, 0x4b800000, v131
	v_cmp_gt_f32_e32 vcc, s61, v131
	s_nop 1
	v_cndmask_b32_e32 v131, v131, v144, vcc
	v_rsq_f32_e32 v131, v131
	s_nop 0
	v_mul_f32_e32 v144, 0x45800000, v131
	v_cndmask_b32_e32 v144, v131, v144, vcc
	v_mul_f32_e64 v228, v144, -v145
	v_pk_fma_f32 v[230:231], v[80:81], v[144:145], v[228:229] op_sel_hi:[1,0,0]
	v_pk_fma_f32 v[232:233], v[78:79], v[144:145], v[228:229] op_sel_hi:[1,0,0]
	v_pk_fma_f32 v[234:235], v[76:77], v[144:145], v[228:229] op_sel_hi:[1,0,0]
	v_pk_fma_f32 v[236:237], v[74:75], v[144:145], v[228:229] op_sel_hi:[1,0,0]
	v_pk_fma_f32 v[238:239], v[72:73], v[144:145], v[228:229] op_sel_hi:[1,0,0]
	v_pk_fma_f32 v[240:241], v[70:71], v[144:145], v[228:229] op_sel_hi:[1,0,0]
	v_pk_fma_f32 v[242:243], v[68:69], v[144:145], v[228:229] op_sel_hi:[1,0,0]
	v_pk_fma_f32 v[244:245], v[66:67], v[144:145], v[228:229] op_sel_hi:[1,0,0]
	v_pk_fma_f32 v[196:197], v[242:243], v[214:215], v[196:197]
	v_pk_fma_f32 v[194:195], v[244:245], v[212:213], v[194:195]
	v_pk_fma_f32 v[132:133], v[240:241], v[132:133], v[140:141]
	v_pk_fma_f32 v[134:135], v[238:239], v[134:135], v[142:143]
	v_pk_fma_f32 v[136:137], v[236:237], v[136:137], v[190:191]
	v_pk_fma_f32 v[138:139], v[234:235], v[138:139], v[192:193]
	v_pk_fma_f32 v[140:141], v[232:233], v[198:199], v[202:203]
	v_pk_fma_f32 v[142:143], v[230:231], v[200:201], v[204:205]
	v_pk_fma_f32 v[14:15], v[130:131], v[140:141], v[14:15] op_sel_hi:[0,1,1]
	v_pk_fma_f32 v[16:17], v[130:131], v[142:143], v[16:17] op_sel_hi:[0,1,1]
	v_pk_fma_f32 v[12:13], v[130:131], v[138:139], v[12:13] op_sel_hi:[0,1,1]
	v_pk_fma_f32 v[10:11], v[130:131], v[136:137], v[10:11] op_sel_hi:[0,1,1]
	v_pk_fma_f32 v[8:9], v[130:131], v[134:135], v[8:9] op_sel_hi:[0,1,1]
	v_pk_fma_f32 v[6:7], v[130:131], v[132:133], v[6:7] op_sel_hi:[0,1,1]
	v_pk_fma_f32 v[4:5], v[130:131], v[196:197], v[4:5] op_sel_hi:[0,1,1]
	v_pk_fma_f32 v[2:3], v[130:131], v[194:195], v[2:3] op_sel_hi:[0,1,1]
	ds_read_b128 v[132:135], v189 offset:33408
	ds_read_b128 v[136:139], v189 offset:33440
	ds_read_b128 v[140:143], v189 offset:33920
	ds_read_b128 v[190:193], v189 offset:33952
	ds_read_b128 v[194:197], v189 offset:33472
	ds_read_b128 v[198:201], v189 offset:33504
	ds_read_b128 v[202:205], v189 offset:33984
	ds_read_b128 v[212:215], v189 offset:34016
	v_pk_fma_f32 v[230:231], v[96:97], v[144:145], v[228:229] op_sel_hi:[1,0,0]
	v_pk_fma_f32 v[232:233], v[94:95], v[144:145], v[228:229] op_sel_hi:[1,0,0]
	v_pk_fma_f32 v[234:235], v[92:93], v[144:145], v[228:229] op_sel_hi:[1,0,0]
	v_pk_fma_f32 v[236:237], v[90:91], v[144:145], v[228:229] op_sel_hi:[1,0,0]
	v_pk_fma_f32 v[238:239], v[88:89], v[144:145], v[228:229] op_sel_hi:[1,0,0]
	v_pk_fma_f32 v[240:241], v[86:87], v[144:145], v[228:229] op_sel_hi:[1,0,0]
	v_pk_fma_f32 v[242:243], v[84:85], v[144:145], v[228:229] op_sel_hi:[1,0,0]
	v_pk_fma_f32 v[244:245], v[82:83], v[144:145], v[228:229] op_sel_hi:[1,0,0]
	s_waitcnt lgkmcnt(5)
	v_pk_fma_f32 v[134:135], v[242:243], v[134:135], v[142:143]
	v_pk_fma_f32 v[132:133], v[244:245], v[132:133], v[140:141]
	s_waitcnt lgkmcnt(4)
	v_pk_fma_f32 v[136:137], v[240:241], v[136:137], v[190:191]
	v_pk_fma_f32 v[138:139], v[238:239], v[138:139], v[192:193]
	s_waitcnt lgkmcnt(1)
	v_pk_fma_f32 v[140:141], v[236:237], v[194:195], v[202:203]
	v_pk_fma_f32 v[142:143], v[234:235], v[196:197], v[204:205]
	s_waitcnt lgkmcnt(0)
	v_pk_fma_f32 v[190:191], v[232:233], v[198:199], v[212:213]
	v_pk_fma_f32 v[192:193], v[230:231], v[200:201], v[214:215]
	v_pk_fma_f32 v[62:63], v[130:131], v[190:191], v[62:63] op_sel_hi:[0,1,1]
	v_pk_fma_f32 v[64:65], v[130:131], v[192:193], v[64:65] op_sel_hi:[0,1,1]
	v_pk_fma_f32 v[60:61], v[130:131], v[142:143], v[60:61] op_sel_hi:[0,1,1]
	v_pk_fma_f32 v[58:59], v[130:131], v[140:141], v[58:59] op_sel_hi:[0,1,1]
	v_pk_fma_f32 v[56:57], v[130:131], v[138:139], v[56:57] op_sel_hi:[0,1,1]
	v_pk_fma_f32 v[54:55], v[130:131], v[136:137], v[54:55] op_sel_hi:[0,1,1]
	v_pk_fma_f32 v[52:53], v[130:131], v[134:135], v[52:53] op_sel_hi:[0,1,1]
	v_pk_fma_f32 v[50:51], v[130:131], v[132:133], v[50:51] op_sel_hi:[0,1,1]
	ds_read_b128 v[132:135], v189 offset:33536
	ds_read_b128 v[136:139], v189 offset:33568
	ds_read_b128 v[140:143], v189 offset:34048
	ds_read_b128 v[190:193], v189 offset:34080
	ds_read_b128 v[194:197], v189 offset:33600
	ds_read_b128 v[198:201], v189 offset:33632
	ds_read_b128 v[202:205], v189 offset:34112
	ds_read_b128 v[212:215], v189 offset:34144
	v_pk_fma_f32 v[230:231], v[112:113], v[144:145], v[228:229] op_sel_hi:[1,0,0]
	v_pk_fma_f32 v[232:233], v[110:111], v[144:145], v[228:229] op_sel_hi:[1,0,0]
	v_pk_fma_f32 v[234:235], v[108:109], v[144:145], v[228:229] op_sel_hi:[1,0,0]
	v_pk_fma_f32 v[236:237], v[106:107], v[144:145], v[228:229] op_sel_hi:[1,0,0]
	v_pk_fma_f32 v[238:239], v[104:105], v[144:145], v[228:229] op_sel_hi:[1,0,0]
	v_pk_fma_f32 v[240:241], v[102:103], v[144:145], v[228:229] op_sel_hi:[1,0,0]
	v_pk_fma_f32 v[242:243], v[100:101], v[144:145], v[228:229] op_sel_hi:[1,0,0]
	v_pk_fma_f32 v[244:245], v[98:99], v[144:145], v[228:229] op_sel_hi:[1,0,0]
	s_waitcnt lgkmcnt(5)
	v_pk_fma_f32 v[134:135], v[242:243], v[134:135], v[142:143]
	v_pk_fma_f32 v[132:133], v[244:245], v[132:133], v[140:141]
	s_waitcnt lgkmcnt(4)
	v_pk_fma_f32 v[136:137], v[240:241], v[136:137], v[190:191]
	v_pk_fma_f32 v[138:139], v[238:239], v[138:139], v[192:193]
	s_waitcnt lgkmcnt(1)
	v_pk_fma_f32 v[140:141], v[236:237], v[194:195], v[202:203]
	v_pk_fma_f32 v[142:143], v[234:235], v[196:197], v[204:205]
	s_waitcnt lgkmcnt(0)
	v_pk_fma_f32 v[190:191], v[232:233], v[198:199], v[212:213]
	v_pk_fma_f32 v[192:193], v[230:231], v[200:201], v[214:215]
	v_pk_fma_f32 v[46:47], v[130:131], v[190:191], v[46:47] op_sel_hi:[0,1,1]
	v_pk_fma_f32 v[48:49], v[130:131], v[192:193], v[48:49] op_sel_hi:[0,1,1]
	v_pk_fma_f32 v[44:45], v[130:131], v[142:143], v[44:45] op_sel_hi:[0,1,1]
	v_pk_fma_f32 v[42:43], v[130:131], v[140:141], v[42:43] op_sel_hi:[0,1,1]
	v_pk_fma_f32 v[40:41], v[130:131], v[138:139], v[40:41] op_sel_hi:[0,1,1]
	v_pk_fma_f32 v[38:39], v[130:131], v[136:137], v[38:39] op_sel_hi:[0,1,1]
	v_pk_fma_f32 v[36:37], v[130:131], v[134:135], v[36:37] op_sel_hi:[0,1,1]
	v_pk_fma_f32 v[34:35], v[130:131], v[132:133], v[34:35] op_sel_hi:[0,1,1]
	ds_read_b128 v[132:135], v189 offset:33664
	ds_read_b128 v[136:139], v189 offset:33696
	ds_read_b128 v[140:143], v189 offset:34176
	ds_read_b128 v[190:193], v189 offset:34208
	ds_read_b128 v[194:197], v189 offset:33728
	ds_read_b128 v[198:201], v189 offset:33760
	ds_read_b128 v[202:205], v189 offset:34240
	ds_read_b128 v[212:215], v189 offset:34272
	v_pk_fma_f32 v[230:231], v[128:129], v[144:145], v[228:229] op_sel_hi:[1,0,0]
	v_pk_fma_f32 v[232:233], v[126:127], v[144:145], v[228:229] op_sel_hi:[1,0,0]
	v_pk_fma_f32 v[234:235], v[124:125], v[144:145], v[228:229] op_sel_hi:[1,0,0]
	v_pk_fma_f32 v[236:237], v[122:123], v[144:145], v[228:229] op_sel_hi:[1,0,0]
	v_pk_fma_f32 v[238:239], v[120:121], v[144:145], v[228:229] op_sel_hi:[1,0,0]
	v_pk_fma_f32 v[240:241], v[118:119], v[144:145], v[228:229] op_sel_hi:[1,0,0]
	v_pk_fma_f32 v[242:243], v[116:117], v[144:145], v[228:229] op_sel_hi:[1,0,0]
	v_pk_fma_f32 v[144:145], v[114:115], v[144:145], v[228:229] op_sel_hi:[1,0,0]
	s_waitcnt lgkmcnt(5)
	v_pk_fma_f32 v[134:135], v[242:243], v[134:135], v[142:143]
	v_pk_fma_f32 v[132:133], v[144:145], v[132:133], v[140:141]
	s_waitcnt lgkmcnt(4)
	v_pk_fma_f32 v[136:137], v[240:241], v[136:137], v[190:191]
	v_pk_fma_f32 v[138:139], v[238:239], v[138:139], v[192:193]
	s_waitcnt lgkmcnt(1)
	v_pk_fma_f32 v[140:141], v[236:237], v[194:195], v[202:203]
	v_pk_fma_f32 v[142:143], v[234:235], v[196:197], v[204:205]
	s_waitcnt lgkmcnt(0)
	v_pk_fma_f32 v[144:145], v[232:233], v[198:199], v[212:213]
	v_pk_fma_f32 v[190:191], v[230:231], v[200:201], v[214:215]
	v_pk_fma_f32 v[30:31], v[130:131], v[144:145], v[30:31] op_sel_hi:[0,1,1]
	v_pk_fma_f32 v[32:33], v[130:131], v[190:191], v[32:33] op_sel_hi:[0,1,1]
	v_pk_fma_f32 v[28:29], v[130:131], v[142:143], v[28:29] op_sel_hi:[0,1,1]
	v_pk_fma_f32 v[26:27], v[130:131], v[140:141], v[26:27] op_sel_hi:[0,1,1]
	v_pk_fma_f32 v[24:25], v[130:131], v[138:139], v[24:25] op_sel_hi:[0,1,1]
	v_pk_fma_f32 v[22:23], v[130:131], v[136:137], v[22:23] op_sel_hi:[0,1,1]
	v_pk_fma_f32 v[20:21], v[130:131], v[134:135], v[20:21] op_sel_hi:[0,1,1]
	v_pk_fma_f32 v[18:19], v[130:131], v[132:133], v[18:19] op_sel_hi:[0,1,1]

	.amdhsa_kernel _Z10ple_kernelPKfPKDv8_DF16_PKcS0_S0_S0_S0_S0_S0_Pf
		.amdhsa_group_segment_fixed_size 0
		.amdhsa_private_segment_fixed_size 0
		.amdhsa_kernarg_size 80
		.amdhsa_user_sgpr_count 2
		.amdhsa_user_sgpr_dispatch_ptr 0
		.amdhsa_user_sgpr_queue_ptr 0
		.amdhsa_user_sgpr_kernarg_segment_ptr 1
		.amdhsa_user_sgpr_dispatch_id 0
		.amdhsa_user_sgpr_kernarg_preload_length 0
		.amdhsa_user_sgpr_kernarg_preload_offset 0
		.amdhsa_user_sgpr_private_segment_size 0
		.amdhsa_uses_dynamic_stack 0
		.amdhsa_enable_private_segment 0
		.amdhsa_system_sgpr_workgroup_id_x 1
		.amdhsa_system_sgpr_workgroup_id_y 0
		.amdhsa_system_sgpr_workgroup_id_z 0
		.amdhsa_system_sgpr_workgroup_info 0
		.amdhsa_system_vgpr_workitem_id 0
		.amdhsa_next_free_vgpr 249
		.amdhsa_next_free_sgpr 63
		.amdhsa_accum_offset 252
		.amdhsa_reserve_vcc 1
		.amdhsa_float_round_mode_32 0
		.amdhsa_float_round_mode_16_64 0
		.amdhsa_float_denorm_mode_32 3
		.amdhsa_float_denorm_mode_16_64 3
		.amdhsa_dx10_clamp 1
		.amdhsa_ieee_mode 1
		.amdhsa_fp16_overflow 0
		.amdhsa_tg_split 0
		.amdhsa_exception_fp_ieee_invalid_op 0
		.amdhsa_exception_fp_denorm_src 0
		.amdhsa_exception_fp_ieee_div_zero 0
		.amdhsa_exception_fp_ieee_overflow 0
		.amdhsa_exception_fp_ieee_underflow 0
		.amdhsa_exception_fp_ieee_inexact 0
		.amdhsa_exception_int_div_zero 0
	.end_amdhsa_kernel

amdhsa.kernels:
  - .agpr_count:     0
    .args:
      - .actual_access:  read_only
        .address_space:  global
        .offset:         0
        .size:           8
        .value_kind:     global_buffer
      - .actual_access:  read_only
        .address_space:  global
        .offset:         8
        .size:           8
        .value_kind:     global_buffer
      - .actual_access:  read_only
        .address_space:  global
        .offset:         16
        .size:           8
        .value_kind:     global_buffer
      - .actual_access:  read_only
        .address_space:  global
        .offset:         24
        .size:           8
        .value_kind:     global_buffer
      - .actual_access:  read_only
        .address_space:  global
        .offset:         32
        .size:           8
        .value_kind:     global_buffer
      - .actual_access:  read_only
        .address_space:  global
        .offset:         40
        .size:           8
        .value_kind:     global_buffer
      - .actual_access:  read_only
        .address_space:  global
        .offset:         48
        .size:           8
        .value_kind:     global_buffer
      - .actual_access:  read_only
        .address_space:  global
        .offset:         56
        .size:           8
        .value_kind:     global_buffer
      - .actual_access:  read_only
        .address_space:  global
        .offset:         64
        .size:           8
        .value_kind:     global_buffer
      - .actual_access:  read_only
        .address_space:  global
        .offset:         72
        .size:           8
        .value_kind:     global_buffer
      - .actual_access:  write_only
        .address_space:  global
        .offset:         80
        .size:           8
        .value_kind:     global_buffer
      - .actual_access:  write_only
        .address_space:  global
        .offset:         88
        .size:           8
        .value_kind:     global_buffer
    .group_segment_fixed_size: 0
    .kernarg_segment_align: 8
    .kernarg_segment_size: 96
    .language:       OpenCL C
    .language_version:
      - 2
      - 0
    .max_flat_workgroup_size: 1024
    .name:           _Z11prep_kernelPKfS0_S0_S0_S0_S0_S0_S0_S0_S0_PDv8_DF16_S2_
    .private_segment_fixed_size: 0
    .sgpr_count:     34
    .sgpr_spill_count: 0
    .symbol:         _Z11prep_kernelPKfS0_S0_S0_S0_S0_S0_S0_S0_S0_PDv8_DF16_S2_.kd
    .uniform_work_group_size: 1
    .uses_dynamic_stack: false
    .vgpr_count:     23
    .vgpr_spill_count: 0
    .wavefront_size: 64
  - .agpr_count:     0
    .args:
      - .actual_access:  read_only
        .address_space:  global
        .offset:         0
        .size:           8
        .value_kind:     global_buffer
      - .actual_access:  read_only
        .address_space:  global
        .offset:         8
        .size:           8
        .value_kind:     global_buffer
      - .address_space:  global
        .offset:         16
        .size:           8
        .value_kind:     global_buffer
      - .actual_access:  read_only
        .address_space:  global
        .offset:         24
        .size:           8
        .value_kind:     global_buffer
      - .actual_access:  read_only
        .address_space:  global
        .offset:         32
        .size:           8
        .value_kind:     global_buffer
      - .actual_access:  read_only
        .address_space:  global
        .offset:         40
        .size:           8
        .value_kind:     global_buffer
      - .actual_access:  read_only
        .address_space:  global
        .offset:         48
        .size:           8
        .value_kind:     global_buffer
      - .actual_access:  read_only
        .address_space:  global
        .offset:         56
        .size:           8
        .value_kind:     global_buffer
      - .actual_access:  read_only
        .address_space:  global
        .offset:         64
        .size:           8
        .value_kind:     global_buffer
      - .actual_access:  write_only
        .address_space:  global
        .offset:         72
        .size:           8
        .value_kind:     global_buffer
    .group_segment_fixed_size: 0
    .kernarg_segment_align: 8
    .kernarg_segment_size: 80
    .language:       OpenCL C
    .language_version:
      - 2
      - 0
    .max_flat_workgroup_size: 512
    .name:           _Z10ple_kernelPKfPKDv8_DF16_PKcS0_S0_S0_S0_S0_S0_Pf
    .private_segment_fixed_size: 0
    .sgpr_count:     69
    .sgpr_spill_count: 0
    .symbol:         _Z10ple_kernelPKfPKDv8_DF16_PKcS0_S0_S0_S0_S0_S0_Pf.kd
    .uniform_work_group_size: 1
    .uses_dynamic_stack: false
    .vgpr_count:     249
    .vgpr_spill_count: 0
    .wavefront_size: 64
